# mixer phases: 4 of every 8 workgroup rows (instead of 3) start on the expert-weight conversion queue
# baseline (speedup 1.0000x reference)
.LBB0_553:
	s_cmp_lt_i32 s42, 4
	s_cselect_b64 s[4:5], -1, 0
	s_cmp_gt_i32 s43, 3
	s_cselect_b64 s[6:7], -1, 0
	s_and_b64 s[4:5], s[4:5], s[6:7]
	s_andn2_b64 vcc, exec, s[4:5]
	s_cbranch_vccnz .LBB0_862
	s_and_b32 s4, s2, 56
	s_cmp_gt_u32 s4, 31
	s_waitcnt lgkmcnt(0)
	s_cselect_b64 s[8:9], -1, 0
	s_and_b64 vcc, exec, s[8:9]
	v_mov_b32 v1, v0
	s_nop 0
	v_mov_b32 v1, v0
	s_nop 0
	v_mov_b32 v1, v0
	s_cbranch_vccnz .LBB0_569
	s_add_u32 s4, s40, 0x6800
	s_addc_u32 s5, s41, 0
	s_and_saveexec_b64 s[6:7], s[36:37]
	s_cbranch_execz .LBB0_559
	s_mov_b64 s[12:13], exec
	v_mbcnt_lo_u32_b32 v1, s12, 0
	v_mbcnt_hi_u32_b32 v1, s13, v1
	v_cmp_eq_u32_e32 vcc, 0, v1
	s_and_saveexec_b64 s[10:11], vcc
	s_cbranch_execz .LBB0_558
	s_bcnt1_i32_b64 s12, s[12:13]
	v_mov_b32_e32 v2, 0
	s_waitcnt vmcnt(0)
	v_mov_b32_e32 v3, s12
	global_atomic_add v2, v2, v3, s[4:5] sc0

.LBB0_922:
	s_cmp_lt_i32 s42, 6
	s_cselect_b64 s[4:5], -1, 0
	s_cmp_gt_i32 s43, 5
	s_cselect_b64 s[6:7], -1, 0
	s_and_b64 s[4:5], s[4:5], s[6:7]
	s_andn2_b64 vcc, exec, s[4:5]
	s_cbranch_vccnz .LBB0_1504
	s_and_b32 s4, s2, 56
	s_cmp_gt_u32 s4, 31
	s_cselect_b64 s[46:47], -1, 0
	s_and_b64 vcc, exec, s[46:47]
	v_mov_b32 v1, v0
	s_nop 0
	v_mov_b32 v1, v0
	s_nop 0
	v_mov_b32 v1, v0
	s_cbranch_vccnz .LBB0_943
	s_add_u32 s4, s40, 0x6900
	s_addc_u32 s5, s41, 0
	s_and_saveexec_b64 s[6:7], s[36:37]
	s_cbranch_execz .LBB0_928
	s_mov_b64 s[10:11], exec
	v_mbcnt_lo_u32_b32 v1, s10, 0
	v_mbcnt_hi_u32_b32 v1, s11, v1
	v_cmp_eq_u32_e32 vcc, 0, v1
	s_waitcnt lgkmcnt(0)
	s_and_saveexec_b64 s[8:9], vcc
	s_cbranch_execz .LBB0_927
	s_bcnt1_i32_b64 s10, s[10:11]
	v_mov_b32_e32 v2, 0
	s_waitcnt vmcnt(0)
	v_mov_b32_e32 v3, s10
	global_atomic_add v2, v2, v3, s[4:5] sc0

.LBB0_2279:
	s_cmp_lt_i32 s42, 14
	s_cselect_b64 s[4:5], -1, 0
	s_cmp_gt_i32 s43, 13
	s_cselect_b64 s[6:7], -1, 0
	s_and_b64 s[4:5], s[4:5], s[6:7]
	s_andn2_b64 vcc, exec, s[4:5]
	s_cbranch_vccnz .LBB0_2588
	s_and_b32 s4, s2, 56
	s_cmp_gt_u32 s4, 31
	s_waitcnt lgkmcnt(0)
	s_cselect_b64 s[8:9], -1, 0
	s_and_b64 vcc, exec, s[8:9]
	v_mov_b32 v1, v0
	s_nop 0
	v_mov_b32 v1, v0
	s_nop 0
	v_mov_b32 v1, v0
	s_cbranch_vccnz .LBB0_2295
	s_add_u32 s4, s40, 0x6a00
	s_addc_u32 s5, s41, 0
	s_and_saveexec_b64 s[6:7], s[36:37]
	s_cbranch_execz .LBB0_2285
	s_mov_b64 s[12:13], exec
	v_mbcnt_lo_u32_b32 v1, s12, 0
	v_mbcnt_hi_u32_b32 v1, s13, v1
	v_cmp_eq_u32_e32 vcc, 0, v1
	s_and_saveexec_b64 s[10:11], vcc
	s_cbranch_execz .LBB0_2284
	s_bcnt1_i32_b64 s12, s[12:13]
	v_mov_b32_e32 v2, 0
	s_waitcnt vmcnt(0)
	v_mov_b32_e32 v3, s12
	global_atomic_add v2, v2, v3, s[4:5] sc0

.LBB0_2648:
	s_cmp_lt_i32 s42, 16
	s_cselect_b64 s[4:5], -1, 0
	s_cmp_gt_i32 s43, 15
	s_cselect_b64 s[6:7], -1, 0
	s_and_b64 s[4:5], s[4:5], s[6:7]
	s_andn2_b64 vcc, exec, s[4:5]
	s_cbranch_vccnz .LBB0_3018
	s_and_b32 s4, s2, 56
	s_cmp_gt_u32 s4, 31
	s_cselect_b64 s[46:47], -1, 0
	s_and_b64 vcc, exec, s[46:47]
	v_mov_b32 v1, v0
	s_nop 0
	v_mov_b32 v1, v0
	s_nop 0
	v_mov_b32 v1, v0
	s_cbranch_vccnz .LBB0_2669
	s_add_u32 s4, s40, 0x6b00
	s_addc_u32 s5, s41, 0
	s_and_saveexec_b64 s[6:7], s[36:37]
	s_cbranch_execz .LBB0_2654
	s_mov_b64 s[10:11], exec
	v_mbcnt_lo_u32_b32 v1, s10, 0
	v_mbcnt_hi_u32_b32 v1, s11, v1
	v_cmp_eq_u32_e32 vcc, 0, v1
	s_waitcnt lgkmcnt(0)
	s_and_saveexec_b64 s[8:9], vcc
	s_cbranch_execz .LBB0_2653
	s_bcnt1_i32_b64 s10, s[10:11]
	v_mov_b32_e32 v2, 0
	s_waitcnt vmcnt(0)
	v_mov_b32_e32 v3, s10
	global_atomic_add v2, v2, v3, s[4:5] sc0
